# hazard fixes on the stack: top-3 compares ordered so each mask is written 2+ instructions before its select; EpiRes shuffle-index select padded likewise
# speedup vs baseline: 1.0016x; 1.0016x over previous
; #define LAS __attribute__((address_space(3)))
; __global__ void __launch_bounds__(NWAVES * 64, 2) mk_fwd(Args args) {
;     ...
;                         float v0 = -INFINITY, v1 = -INFINITY, v2 = -INFINITY; int i0 = -1, i1 = -1, i2 = -1;
; #pragma unroll 1
;                         for (int n = 0; n < qb_; ++n) {
;                             const LAS float* kp = km + n * 136 + half * 68;
;                             float a0 = 0.f, a1 = 0.f, a2 = 0.f, a3 = 0.f;
; #pragma unroll
;                             for (int jj = 0; jj < 64; jj += 4) { const f32x4 kv = *(const LAS f32x4*)(kp + jj);
;                                 a0 += q[jj] * kv[0]; a1 += q[jj + 1] * kv[1]; a2 += q[jj + 2] * kv[2]; a3 += q[jj + 3] * kv[3]; }
;                             float gsc = (a0 + a1) + (a2 + a3); gsc += __shfl_xor(gsc, 1);
;                             if (gsc > v0) { v2 = v1; i2 = i1; v1 = v0; i1 = i0; v0 = gsc; i0 = n; }
;                             else if (gsc > v1) { v2 = v1; i2 = i1; v1 = gsc; i1 = n; }
;                             else if (gsc > v2) { v2 = gsc; i2 = n; }
;                         }
.Lpa_loop:
	v_add_u32_e32 v127, s36, v88
	ds_read_b128 v[92:95], v127
	ds_read_b128 v[96:99], v127 offset:16
	ds_read_b128 v[100:103], v127 offset:32
	ds_read_b128 v[104:107], v127 offset:48
	ds_read_b128 v[108:111], v127 offset:64
	ds_read_b128 v[112:115], v127 offset:80
	ds_read_b128 v[116:119], v127 offset:96
	ds_read_b128 v[120:123], v127 offset:112
	s_waitcnt lgkmcnt(7)
	v_pk_fma_f32 v[130:131], v[10:11], v[92:93], 0 op_sel_hi:[1,1,0]
	v_pk_fma_f32 v[132:133], v[12:13], v[94:95], 0 op_sel_hi:[1,1,0]
	ds_read_b128 v[92:95], v127 offset:128
	s_waitcnt lgkmcnt(7)
	v_pk_fma_f32 v[130:131], v[14:15], v[96:97], v[130:131]
	v_pk_fma_f32 v[132:133], v[16:17], v[98:99], v[132:133]
	ds_read_b128 v[96:99], v127 offset:144
	s_waitcnt lgkmcnt(7)
	v_pk_fma_f32 v[130:131], v[18:19], v[100:101], v[130:131]
	v_pk_fma_f32 v[132:133], v[20:21], v[102:103], v[132:133]
	ds_read_b128 v[100:103], v127 offset:160
	s_waitcnt lgkmcnt(7)
	v_pk_fma_f32 v[130:131], v[22:23], v[104:105], v[130:131]
	v_pk_fma_f32 v[132:133], v[24:25], v[106:107], v[132:133]
	ds_read_b128 v[104:107], v127 offset:176
	s_waitcnt lgkmcnt(7)
	v_pk_fma_f32 v[130:131], v[26:27], v[108:109], v[130:131]
	v_pk_fma_f32 v[132:133], v[28:29], v[110:111], v[132:133]
	ds_read_b128 v[108:111], v127 offset:192
	s_waitcnt lgkmcnt(7)
	v_pk_fma_f32 v[130:131], v[30:31], v[112:113], v[130:131]
	v_pk_fma_f32 v[132:133], v[32:33], v[114:115], v[132:133]
	ds_read_b128 v[112:115], v127 offset:208
	s_waitcnt lgkmcnt(7)
	v_pk_fma_f32 v[130:131], v[34:35], v[116:117], v[130:131]
	v_pk_fma_f32 v[132:133], v[36:37], v[118:119], v[132:133]
	ds_read_b128 v[116:119], v127 offset:224
	s_waitcnt lgkmcnt(7)
	v_pk_fma_f32 v[130:131], v[38:39], v[120:121], v[130:131]
	v_pk_fma_f32 v[132:133], v[40:41], v[122:123], v[132:133]
	ds_read_b128 v[120:123], v127 offset:240
	s_waitcnt lgkmcnt(7)
	v_pk_fma_f32 v[130:131], v[42:43], v[92:93], v[130:131]
	v_pk_fma_f32 v[132:133], v[44:45], v[94:95], v[132:133]
	s_waitcnt lgkmcnt(6)
	v_pk_fma_f32 v[130:131], v[46:47], v[96:97], v[130:131]
	v_pk_fma_f32 v[132:133], v[48:49], v[98:99], v[132:133]
	s_waitcnt lgkmcnt(5)
	v_pk_fma_f32 v[130:131], v[50:51], v[100:101], v[130:131]
	v_pk_fma_f32 v[132:133], v[52:53], v[102:103], v[132:133]
	s_waitcnt lgkmcnt(4)
	v_pk_fma_f32 v[130:131], v[54:55], v[104:105], v[130:131]
	v_pk_fma_f32 v[132:133], v[56:57], v[106:107], v[132:133]
	s_waitcnt lgkmcnt(3)
	v_pk_fma_f32 v[130:131], v[58:59], v[108:109], v[130:131]
	v_pk_fma_f32 v[132:133], v[60:61], v[110:111], v[132:133]
	s_waitcnt lgkmcnt(2)
	v_pk_fma_f32 v[130:131], v[62:63], v[112:113], v[130:131]
	v_pk_fma_f32 v[132:133], v[64:65], v[114:115], v[132:133]
	s_waitcnt lgkmcnt(1)
	v_pk_fma_f32 v[130:131], v[66:67], v[116:117], v[130:131]
	v_pk_fma_f32 v[132:133], v[68:69], v[118:119], v[132:133]
	s_waitcnt lgkmcnt(0)
	v_pk_fma_f32 v[130:131], v[70:71], v[120:121], v[130:131]
	v_pk_fma_f32 v[132:133], v[72:73], v[122:123], v[132:133]
	v_add_f32_e32 v134, v130, v131
	v_add_f32_e32 v135, v132, v133
	v_mov_b32_e32 v136, s37
	v_add_f32_e32 v134, v134, v135
	s_nop 1
	v_mov_b32_dpp v135, v134 quad_perm:[1,0,3,2] row_mask:0xf bank_mask:0xf
	s_add_i32 s37, s37, 1
	s_addk_i32 s36, 0x220
	v_add_f32_e32 v134, v134, v135
	v_cmp_gt_f32_e64 s[16:17], v134, v126
	v_cmp_gt_f32_e64 s[14:15], v134, v125
	v_cmp_gt_f32_e64 s[12:13], v134, v124
	v_cndmask_b32_e64 v126, v126, v134, s[16:17]
	v_cndmask_b32_e64 v83, v83, v136, s[16:17]
	v_cndmask_b32_e64 v126, v126, v125, s[14:15]
	v_cndmask_b32_e64 v83, v83, v84, s[14:15]
	v_cndmask_b32_e64 v125, v125, v134, s[14:15]
	v_cndmask_b32_e64 v84, v84, v136, s[14:15]
	v_cndmask_b32_e64 v125, v125, v124, s[12:13]
	v_cndmask_b32_e64 v84, v84, v85, s[12:13]
	v_cndmask_b32_e64 v124, v124, v134, s[12:13]
	v_cndmask_b32_e64 v85, v85, v136, s[12:13]
	s_cmp_eq_u32 s37, s35
	s_cbranch_scc0 .Lpa_loop

; __device__ __forceinline__ unsigned cvt_pk_bf16(float lo, float hi) { const f32x2_t v = {lo, hi}; const bf16x2_t b = __builtin_convertvector(v, bf16x2_t); return __builtin_bit_cast(unsigned, b); }
; #define EPIRES_LOAD(buf, g) do { _Pragma("unroll") for (int bj = 0; bj < 2; ++bj) xb[buf][bj] = *(const u32x4*)(x + EPIRES_OFF(g, bj)); } while (0)
;     __device__ __forceinline__ void operator()(const f32x4 (&acc)[2][2][4][2], const Unit& u, int wr, int wc, int fr, int fq, int ui) const {
;         const int col0 = u.pn * BM + wc * 32 + 8 * fq;
;         const size_t off0 = ((size_t)(u.pm * (D / 64) + (col0 >> 6)) * 256 + wr * 64 + fr) * 64 + (col0 & 63);
;         f32x4 cr[2][2];
; #pragma unroll
;         for (int bj = 0; bj < 2; ++bj)
; #pragma unroll
;             for (int n = 0; n < 2; ++n) cr[bj][n] = *(const f32x4*)(cres + col0 + bj * HALF + n * 4);
;         u32x4 xb[3][2];
;     ...
;         EPIRES_LOAD(0, 0); EPIRES_LOAD(1, 1); EPIRES_LOAD(2, 2);
; #pragma unroll
;         for (int g = 0; g < 8; ++g) {
;             const int ai = g >> 2, m = g & 3;
;             const int row_ = u.pm * BM + ai * HALF + wr * 64 + m * 16 + fr;
;             float sq = 0.f;
; #pragma unroll
;             for (int bj = 0; bj < 2; ++bj) {
;                 u32x4 xs;
; #pragma unroll
;                 for (int n = 0; n < 2; ++n) {
;                     const unsigned p0 = xb[g % 3][bj][2 * n], p1 = xb[g % 3][bj][2 * n + 1];
;                     const f32x4 xo = {__builtin_bit_cast(float, p0 << 16), __builtin_bit_cast(float, p0 & 0xFFFF0000u), __builtin_bit_cast(float, p1 << 16), __builtin_bit_cast(float, p1 & 0xFFFF0000u)};
;                     const f32x4 xn = xo + cr[bj][n] * acc[ai][bj][m][n];
;                     sq += (xn[0] * xn[0] + xn[1] * xn[1]) + (xn[2] * xn[2] + xn[3] * xn[3]);
;                     if (n == 0) { xs.x = cvt_pk_bf16(xn[0], xn[1]); xs.y = cvt_pk_bf16(xn[2], xn[3]); } else { xs.z = cvt_pk_bf16(xn[0], xn[1]); xs.w = cvt_pk_bf16(xn[2], xn[3]); }
;                 }
;                 *(u32x4*)(x + EPIRES_OFF(g, bj)) = xs;
.LBB0_1399:
	s_lshl_b32 s18, s48, 8
	s_or_b32 s20, s18, s39
	s_lshl_b32 s18, s49, 5
	s_ashr_i32 s19, s20, 6
	s_add_i32 s18, s19, s18
	s_ashr_i32 s19, s18, 31
	v_or_b32_e32 v88, s20, v194
	v_bitop3_b32 v128, s20, 56, v194 bitop3:0xc8
	s_lshl_b64 s[18:19], s[18:19], 15
	v_ashrrev_i32_e32 v89, 31, v88
	v_lshl_add_u64 v[146:147], v[186:187], 0, s[18:19]
	v_lshlrev_b32_e32 v128, 1, v128
	v_lshl_add_u64 v[92:93], v[88:89], 2, s[10:11]
	v_lshl_add_u64 v[188:189], v[146:147], 0, v[128:129]
	global_load_dwordx4 v[100:103], v[92:93], off offset:16
	global_load_dwordx4 v[108:111], v[92:93], off
	global_load_dwordx4 v[88:91], v[92:93], off offset:528
	s_nop 0
	global_load_dwordx4 v[92:95], v[92:93], off offset:512
	s_mov_b64 s[20:21], 0x1000
	v_lshl_add_u64 v[172:173], v[188:189], 0, s[20:21]
	s_mov_b64 s[20:21], 0x5000
	v_lshl_add_u64 v[174:175], v[188:189], 0, s[20:21]
	s_mov_b64 s[20:21], 0x11000
	v_lshl_add_u64 v[190:191], v[188:189], 0, s[20:21]
	s_mov_b64 s[20:21], 0x15000
	v_lshl_add_u64 v[192:193], v[188:189], 0, s[20:21]
	global_load_dwordx4 v[146:149], v[172:173], off offset:-4096
	global_load_dwordx4 v[150:153], v[190:191], off offset:-4096
	global_load_dwordx4 v[154:157], v[172:173], off offset:-2048
	global_load_dwordx4 v[158:161], v[190:191], off offset:-2048
	global_load_dwordx4 v[162:165], v[172:173], off
	global_load_dwordx4 v[166:169], v[190:191], off
	global_load_dwordx4 v[196:199], v[172:173], off offset:2048
	global_load_dwordx4 v[200:203], v[190:191], off offset:2048
	global_load_dwordx4 v[204:207], v[174:175], off offset:-4096
	global_load_dwordx4 v[208:211], v[192:193], off offset:-4096
	global_load_dwordx4 v[212:215], v[174:175], off offset:-2048
	global_load_dwordx4 v[216:219], v[192:193], off offset:-2048
	global_load_dwordx4 v[220:223], v[174:175], off
	global_load_dwordx4 v[224:227], v[192:193], off
	s_waitcnt vmcnt(0)
	v_lshlrev_b32_e32 v128, 16, v146
	v_and_b32_e32 v146, 0xffff0000, v146
	v_fma_f32 v142, v142, v108, v128
	v_fma_f32 v143, v143, v109, v146
	v_lshlrev_b32_e32 v128, 16, v147
	v_and_b32_e32 v147, 0xffff0000, v147
	v_fma_f32 v144, v144, v110, v128
	v_fma_f32 v145, v145, v111, v147
	v_mul_f32_e32 v146, v143, v143
	v_mul_f32_e32 v147, v145, v145
	v_fmac_f32_e32 v146, v142, v142
	v_fmac_f32_e32 v147, v144, v144
	v_add_f32_e32 v146, v146, v147
	v_lshlrev_b32_e32 v128, 16, v148
	v_and_b32_e32 v148, 0xffff0000, v148
	v_fma_f32 v138, v138, v100, v128
	v_fma_f32 v139, v139, v101, v148
	v_lshlrev_b32_e32 v128, 16, v149
	v_and_b32_e32 v149, 0xffff0000, v149
	v_fma_f32 v140, v140, v102, v128
	v_fma_f32 v141, v141, v103, v149
	v_mul_f32_e32 v148, v139, v139
	v_mul_f32_e32 v149, v141, v141
	v_fmac_f32_e32 v148, v138, v138
	v_fmac_f32_e32 v149, v140, v140
	v_add_f32_e32 v148, v148, v149
	v_add_f32_e32 v128, v146, v148
	v_cvt_pk_bf16_f32 v146, v142, v143
	v_cvt_pk_bf16_f32 v147, v144, v145
	v_cvt_pk_bf16_f32 v148, v138, v139
	v_cvt_pk_bf16_f32 v149, v140, v141
	v_mov_b32_e32 v142, v128
	global_store_dwordx4 v[172:173], v[146:149], off offset:-4096
	v_lshlrev_b32_e32 v128, 16, v150
	v_and_b32_e32 v150, 0xffff0000, v150
	v_fma_f32 v134, v134, v92, v128
	v_fma_f32 v135, v135, v93, v150
	v_lshlrev_b32_e32 v128, 16, v151
	v_and_b32_e32 v151, 0xffff0000, v151
	v_fma_f32 v136, v136, v94, v128
	v_fma_f32 v137, v137, v95, v151
	v_mul_f32_e32 v150, v135, v135
	v_mul_f32_e32 v151, v137, v137
	v_fmac_f32_e32 v150, v134, v134
	v_fmac_f32_e32 v151, v136, v136
	v_add_f32_e32 v150, v150, v151
	v_lshlrev_b32_e32 v128, 16, v152
	v_and_b32_e32 v152, 0xffff0000, v152
	v_fma_f32 v130, v130, v88, v128
	v_fma_f32 v131, v131, v89, v152
	v_lshlrev_b32_e32 v128, 16, v153
	v_and_b32_e32 v153, 0xffff0000, v153
	v_fma_f32 v132, v132, v90, v128
	v_fma_f32 v133, v133, v91, v153
	v_mul_f32_e32 v152, v131, v131
	v_mul_f32_e32 v153, v133, v133
	v_fmac_f32_e32 v152, v130, v130
	v_fmac_f32_e32 v153, v132, v132
	v_add_f32_e32 v152, v152, v153
	v_add_f32_e32 v128, v142, v150
	v_add_f32_e32 v128, v128, v152
	v_cvt_pk_bf16_f32 v150, v134, v135
	v_cvt_pk_bf16_f32 v151, v136, v137
	v_cvt_pk_bf16_f32 v152, v130, v131
	v_cvt_pk_bf16_f32 v153, v132, v133
	v_mov_b32_e32 v142, v128
	global_store_dwordx4 v[190:191], v[150:153], off offset:-4096
	global_load_dwordx4 v[138:141], v[174:175], off offset:2048
	global_load_dwordx4 v[134:137], v[192:193], off offset:2048
	v_lshlrev_b32_e32 v128, 16, v154
	v_and_b32_e32 v154, 0xffff0000, v154
	v_fma_f32 v124, v124, v108, v128
	v_fma_f32 v125, v125, v109, v154
	v_lshlrev_b32_e32 v128, 16, v155
	v_and_b32_e32 v155, 0xffff0000, v155
	v_fma_f32 v126, v126, v110, v128
	v_fma_f32 v127, v127, v111, v155
	v_mul_f32_e32 v154, v125, v125
	v_mul_f32_e32 v155, v127, v127
	v_fmac_f32_e32 v154, v124, v124
	v_fmac_f32_e32 v155, v126, v126
	v_add_f32_e32 v154, v154, v155
	v_lshlrev_b32_e32 v128, 16, v156
	v_and_b32_e32 v156, 0xffff0000, v156
	v_fma_f32 v120, v120, v100, v128
	v_fma_f32 v121, v121, v101, v156
	v_lshlrev_b32_e32 v128, 16, v157
	v_and_b32_e32 v157, 0xffff0000, v157
	v_fma_f32 v122, v122, v102, v128
	v_fma_f32 v123, v123, v103, v157
	v_mul_f32_e32 v156, v121, v121
	v_mul_f32_e32 v157, v123, v123
	v_fmac_f32_e32 v156, v120, v120
	v_fmac_f32_e32 v157, v122, v122
	v_add_f32_e32 v156, v156, v157
	v_add_f32_e32 v128, v154, v156
	v_cvt_pk_bf16_f32 v154, v124, v125
	v_cvt_pk_bf16_f32 v155, v126, v127
	v_cvt_pk_bf16_f32 v156, v120, v121
	v_cvt_pk_bf16_f32 v157, v122, v123
	v_mov_b32_e32 v124, v128
	global_store_dwordx4 v[172:173], v[154:157], off offset:-2048
	v_lshlrev_b32_e32 v128, 16, v158
	v_and_b32_e32 v158, 0xffff0000, v158
	v_fma_f32 v116, v116, v92, v128
	v_fma_f32 v117, v117, v93, v158
	v_lshlrev_b32_e32 v128, 16, v159
; __device__ __forceinline__ unsigned cvt_pk_bf16(float lo, float hi) { const f32x2_t v = {lo, hi}; const bf16x2_t b = __builtin_convertvector(v, bf16x2_t); return __builtin_bit_cast(unsigned, b); }
;     __device__ __forceinline__ void operator()(const f32x4 (&acc)[2][2][4][2], const Unit& u, int wr, int wc, int fr, int fq, int ui) const {
;     ...
;             for (int bj = 0; bj < 2; ++bj) {
;                 u32x4 xs;
; #pragma unroll
;                 for (int n = 0; n < 2; ++n) {
;                     const unsigned p0 = xb[g % 3][bj][2 * n], p1 = xb[g % 3][bj][2 * n + 1];
;                     const f32x4 xo = {__builtin_bit_cast(float, p0 << 16), __builtin_bit_cast(float, p0 & 0xFFFF0000u), __builtin_bit_cast(float, p1 << 16), __builtin_bit_cast(float, p1 & 0xFFFF0000u)};
;                     const f32x4 xn = xo + cr[bj][n] * acc[ai][bj][m][n];
;                     sq += (xn[0] * xn[0] + xn[1] * xn[1]) + (xn[2] * xn[2] + xn[3] * xn[3]);
;                     if (n == 0) { xs.x = cvt_pk_bf16(xn[0], xn[1]); xs.y = cvt_pk_bf16(xn[2], xn[3]); } else { xs.z = cvt_pk_bf16(xn[0], xn[1]); xs.w = cvt_pk_bf16(xn[2], xn[3]); }
;                 }
;                 *(u32x4*)(x + EPIRES_OFF(g, bj)) = xs;
	v_and_b32_e32 v159, 0xffff0000, v159
	v_fma_f32 v118, v118, v94, v128
	v_fma_f32 v119, v119, v95, v159
	v_mul_f32_e32 v158, v117, v117
	v_mul_f32_e32 v159, v119, v119
	v_fmac_f32_e32 v158, v116, v116
	v_fmac_f32_e32 v159, v118, v118
	v_add_f32_e32 v158, v158, v159
	v_lshlrev_b32_e32 v128, 16, v160
	v_and_b32_e32 v160, 0xffff0000, v160
	v_fma_f32 v112, v112, v88, v128
	v_fma_f32 v113, v113, v89, v160
	v_lshlrev_b32_e32 v128, 16, v161
	v_and_b32_e32 v161, 0xffff0000, v161
	v_fma_f32 v114, v114, v90, v128
	v_fma_f32 v115, v115, v91, v161
	v_mul_f32_e32 v160, v113, v113
	v_mul_f32_e32 v161, v115, v115
	v_fmac_f32_e32 v160, v112, v112
	v_fmac_f32_e32 v161, v114, v114
	v_add_f32_e32 v160, v160, v161
	v_add_f32_e32 v128, v124, v158
	v_add_f32_e32 v128, v128, v160
	v_cvt_pk_bf16_f32 v158, v116, v117
	v_cvt_pk_bf16_f32 v159, v118, v119
	v_cvt_pk_bf16_f32 v160, v112, v113
	v_cvt_pk_bf16_f32 v161, v114, v115
	v_mov_b32_e32 v124, v128
	global_store_dwordx4 v[190:191], v[158:161], off offset:-2048
	v_lshlrev_b32_e32 v128, 16, v162
	v_and_b32_e32 v162, 0xffff0000, v162
	v_fma_f32 v104, v104, v108, v128
	v_fma_f32 v105, v105, v109, v162
	v_lshlrev_b32_e32 v128, 16, v163
	v_and_b32_e32 v163, 0xffff0000, v163
	v_fma_f32 v106, v106, v110, v128
	v_fma_f32 v107, v107, v111, v163
	v_mul_f32_e32 v162, v105, v105
	v_mul_f32_e32 v163, v107, v107
	v_fmac_f32_e32 v162, v104, v104
	v_fmac_f32_e32 v163, v106, v106
	v_add_f32_e32 v162, v162, v163
	v_lshlrev_b32_e32 v128, 16, v164
	v_and_b32_e32 v164, 0xffff0000, v164
	v_fma_f32 v96, v96, v100, v128
	v_fma_f32 v97, v97, v101, v164
	v_lshlrev_b32_e32 v128, 16, v165
	v_and_b32_e32 v165, 0xffff0000, v165
	v_fma_f32 v98, v98, v102, v128
	v_fma_f32 v99, v99, v103, v165
	v_mul_f32_e32 v164, v97, v97
	v_mul_f32_e32 v165, v99, v99
	v_fmac_f32_e32 v164, v96, v96
	v_fmac_f32_e32 v165, v98, v98
	v_add_f32_e32 v164, v164, v165
	v_add_f32_e32 v128, v162, v164
	v_cvt_pk_bf16_f32 v162, v104, v105
	v_cvt_pk_bf16_f32 v163, v106, v107
	v_cvt_pk_bf16_f32 v164, v96, v97
	v_cvt_pk_bf16_f32 v165, v98, v99
	v_mov_b32_e32 v104, v128
	global_store_dwordx4 v[172:173], v[162:165], off
	v_lshlrev_b32_e32 v128, 16, v166
	v_and_b32_e32 v166, 0xffff0000, v166
	v_fma_f32 v84, v84, v92, v128
	v_fma_f32 v85, v85, v93, v166
	v_lshlrev_b32_e32 v128, 16, v167
	v_and_b32_e32 v167, 0xffff0000, v167
	v_fma_f32 v86, v86, v94, v128
	v_fma_f32 v87, v87, v95, v167
	v_mul_f32_e32 v166, v85, v85
	v_mul_f32_e32 v167, v87, v87
	v_fmac_f32_e32 v166, v84, v84
	v_fmac_f32_e32 v167, v86, v86
	v_add_f32_e32 v166, v166, v167
	v_lshlrev_b32_e32 v128, 16, v168
	v_and_b32_e32 v168, 0xffff0000, v168
	v_fma_f32 v80, v80, v88, v128
	v_fma_f32 v81, v81, v89, v168
	v_lshlrev_b32_e32 v128, 16, v169
	v_and_b32_e32 v169, 0xffff0000, v169
	v_fma_f32 v82, v82, v90, v128
	v_fma_f32 v83, v83, v91, v169
	v_mul_f32_e32 v168, v81, v81
	v_mul_f32_e32 v169, v83, v83
	v_fmac_f32_e32 v168, v80, v80
	v_fmac_f32_e32 v169, v82, v82
	v_add_f32_e32 v168, v168, v169
	v_add_f32_e32 v128, v104, v166
	v_add_f32_e32 v128, v128, v168
	v_cvt_pk_bf16_f32 v166, v84, v85
	v_cvt_pk_bf16_f32 v167, v86, v87
	v_cvt_pk_bf16_f32 v168, v80, v81
	v_cvt_pk_bf16_f32 v169, v82, v83
	v_mov_b32_e32 v104, v128
	global_store_dwordx4 v[190:191], v[166:169], off
	v_lshlrev_b32_e32 v128, 16, v196
	v_and_b32_e32 v196, 0xffff0000, v196
	v_fma_f32 v76, v76, v108, v128
	v_fma_f32 v77, v77, v109, v196
	v_lshlrev_b32_e32 v128, 16, v197
	v_and_b32_e32 v197, 0xffff0000, v197
	v_fma_f32 v78, v78, v110, v128
	v_fma_f32 v79, v79, v111, v197
	v_mul_f32_e32 v196, v77, v77
	v_mul_f32_e32 v197, v79, v79
	v_fmac_f32_e32 v196, v76, v76
	v_fmac_f32_e32 v197, v78, v78
	v_add_f32_e32 v196, v196, v197
	v_lshlrev_b32_e32 v128, 16, v198
	v_and_b32_e32 v198, 0xffff0000, v198
	v_fma_f32 v72, v72, v100, v128
	v_fma_f32 v73, v73, v101, v198
	v_lshlrev_b32_e32 v128, 16, v199
	v_and_b32_e32 v199, 0xffff0000, v199
	v_fma_f32 v74, v74, v102, v128
	v_fma_f32 v75, v75, v103, v199
	v_mul_f32_e32 v198, v73, v73
	v_mul_f32_e32 v199, v75, v75
	v_fmac_f32_e32 v198, v72, v72
	v_fmac_f32_e32 v199, v74, v74
	v_add_f32_e32 v198, v198, v199
	v_add_f32_e32 v128, v196, v198
	v_cvt_pk_bf16_f32 v196, v76, v77
	v_cvt_pk_bf16_f32 v197, v78, v79
	v_cvt_pk_bf16_f32 v198, v72, v73
	v_cvt_pk_bf16_f32 v199, v74, v75
	v_mov_b32_e32 v76, v128
	global_store_dwordx4 v[172:173], v[196:199], off offset:2048
	v_lshlrev_b32_e32 v128, 16, v200
	v_and_b32_e32 v200, 0xffff0000, v200
	v_fma_f32 v68, v68, v92, v128
	v_fma_f32 v69, v69, v93, v200
	v_lshlrev_b32_e32 v128, 16, v201
	v_and_b32_e32 v201, 0xffff0000, v201
	v_fma_f32 v70, v70, v94, v128
	v_fma_f32 v71, v71, v95, v201
	v_mul_f32_e32 v200, v69, v69
	v_mul_f32_e32 v201, v71, v71
	v_fmac_f32_e32 v200, v68, v68
	v_fmac_f32_e32 v201, v70, v70
	v_add_f32_e32 v200, v200, v201
	v_lshlrev_b32_e32 v128, 16, v202
	v_and_b32_e32 v202, 0xffff0000, v202
	v_fma_f32 v64, v64, v88, v128
	v_fma_f32 v65, v65, v89, v202
	v_lshlrev_b32_e32 v128, 16, v203
	v_and_b32_e32 v203, 0xffff0000, v203
	v_fma_f32 v66, v66, v90, v128
	v_fma_f32 v67, v67, v91, v203
	v_mul_f32_e32 v202, v65, v65
	v_mul_f32_e32 v203, v67, v67
	v_fmac_f32_e32 v202, v64, v64
	v_fmac_f32_e32 v203, v66, v66
	v_add_f32_e32 v202, v202, v203
	v_add_f32_e32 v128, v76, v200
	v_add_f32_e32 v128, v128, v202
	v_cvt_pk_bf16_f32 v200, v68, v69
	v_cvt_pk_bf16_f32 v201, v70, v71
	v_cvt_pk_bf16_f32 v202, v64, v65
	v_cvt_pk_bf16_f32 v203, v66, v67
	v_mov_b32_e32 v76, v128
	global_store_dwordx4 v[190:191], v[200:203], off offset:2048
	v_lshlrev_b32_e32 v128, 16, v204
	v_and_b32_e32 v204, 0xffff0000, v204
	v_fma_f32 v60, v60, v108, v128
	v_fma_f32 v61, v61, v109, v204
	v_lshlrev_b32_e32 v128, 16, v205
; __device__ __forceinline__ unsigned cvt_pk_bf16(float lo, float hi) { const f32x2_t v = {lo, hi}; const bf16x2_t b = __builtin_convertvector(v, bf16x2_t); return __builtin_bit_cast(unsigned, b); }
;     __device__ __forceinline__ void operator()(const f32x4 (&acc)[2][2][4][2], const Unit& u, int wr, int wc, int fr, int fq, int ui) const {
;     ...
;             for (int bj = 0; bj < 2; ++bj) {
;                 u32x4 xs;
; #pragma unroll
;                 for (int n = 0; n < 2; ++n) {
;                     const unsigned p0 = xb[g % 3][bj][2 * n], p1 = xb[g % 3][bj][2 * n + 1];
;                     const f32x4 xo = {__builtin_bit_cast(float, p0 << 16), __builtin_bit_cast(float, p0 & 0xFFFF0000u), __builtin_bit_cast(float, p1 << 16), __builtin_bit_cast(float, p1 & 0xFFFF0000u)};
;                     const f32x4 xn = xo + cr[bj][n] * acc[ai][bj][m][n];
;                     sq += (xn[0] * xn[0] + xn[1] * xn[1]) + (xn[2] * xn[2] + xn[3] * xn[3]);
;                     if (n == 0) { xs.x = cvt_pk_bf16(xn[0], xn[1]); xs.y = cvt_pk_bf16(xn[2], xn[3]); } else { xs.z = cvt_pk_bf16(xn[0], xn[1]); xs.w = cvt_pk_bf16(xn[2], xn[3]); }
;                 }
;                 *(u32x4*)(x + EPIRES_OFF(g, bj)) = xs;
	v_and_b32_e32 v205, 0xffff0000, v205
	v_fma_f32 v62, v62, v110, v128
	v_fma_f32 v63, v63, v111, v205
	v_mul_f32_e32 v204, v61, v61
	v_mul_f32_e32 v205, v63, v63
	v_fmac_f32_e32 v204, v60, v60
	v_fmac_f32_e32 v205, v62, v62
	v_add_f32_e32 v204, v204, v205
	v_lshlrev_b32_e32 v128, 16, v206
	v_and_b32_e32 v206, 0xffff0000, v206
	v_fma_f32 v56, v56, v100, v128
	v_fma_f32 v57, v57, v101, v206
	v_lshlrev_b32_e32 v128, 16, v207
	v_and_b32_e32 v207, 0xffff0000, v207
	v_fma_f32 v58, v58, v102, v128
	v_fma_f32 v59, v59, v103, v207
	v_mul_f32_e32 v206, v57, v57
	v_mul_f32_e32 v207, v59, v59
	v_fmac_f32_e32 v206, v56, v56
	v_fmac_f32_e32 v207, v58, v58
	v_add_f32_e32 v206, v206, v207
	v_add_f32_e32 v128, v204, v206
	v_cvt_pk_bf16_f32 v204, v60, v61
	v_cvt_pk_bf16_f32 v205, v62, v63
	v_cvt_pk_bf16_f32 v206, v56, v57
	v_cvt_pk_bf16_f32 v207, v58, v59
	v_mov_b32_e32 v60, v128
	global_store_dwordx4 v[174:175], v[204:207], off offset:-4096
	v_lshlrev_b32_e32 v128, 16, v208
	v_and_b32_e32 v208, 0xffff0000, v208
	v_fma_f32 v52, v52, v92, v128
	v_fma_f32 v53, v53, v93, v208
	v_lshlrev_b32_e32 v128, 16, v209
	v_and_b32_e32 v209, 0xffff0000, v209
	v_fma_f32 v54, v54, v94, v128
	v_fma_f32 v55, v55, v95, v209
	v_mul_f32_e32 v208, v53, v53
	v_mul_f32_e32 v209, v55, v55
	v_fmac_f32_e32 v208, v52, v52
	v_fmac_f32_e32 v209, v54, v54
	v_add_f32_e32 v208, v208, v209
	v_lshlrev_b32_e32 v128, 16, v210
	v_and_b32_e32 v210, 0xffff0000, v210
	v_fma_f32 v48, v48, v88, v128
	v_fma_f32 v49, v49, v89, v210
	v_lshlrev_b32_e32 v128, 16, v211
	v_and_b32_e32 v211, 0xffff0000, v211
	v_fma_f32 v50, v50, v90, v128
	v_fma_f32 v51, v51, v91, v211
	v_mul_f32_e32 v210, v49, v49
	v_mul_f32_e32 v211, v51, v51
	v_fmac_f32_e32 v210, v48, v48
	v_fmac_f32_e32 v211, v50, v50
	v_add_f32_e32 v210, v210, v211
	v_add_f32_e32 v128, v60, v208
	v_add_f32_e32 v128, v128, v210
	v_cvt_pk_bf16_f32 v208, v52, v53
	v_cvt_pk_bf16_f32 v209, v54, v55
	v_cvt_pk_bf16_f32 v210, v48, v49
	v_cvt_pk_bf16_f32 v211, v50, v51
	v_mov_b32_e32 v60, v128
	global_store_dwordx4 v[192:193], v[208:211], off offset:-4096
	v_lshlrev_b32_e32 v128, 16, v212
	v_and_b32_e32 v212, 0xffff0000, v212
	v_fma_f32 v44, v44, v108, v128
	v_fma_f32 v45, v45, v109, v212
	v_lshlrev_b32_e32 v128, 16, v213
	v_and_b32_e32 v213, 0xffff0000, v213
	v_fma_f32 v46, v46, v110, v128
	v_fma_f32 v47, v47, v111, v213
	v_mul_f32_e32 v212, v45, v45
	v_mul_f32_e32 v213, v47, v47
	v_fmac_f32_e32 v212, v44, v44
	v_fmac_f32_e32 v213, v46, v46
	v_add_f32_e32 v212, v212, v213
	v_lshlrev_b32_e32 v128, 16, v214
	v_and_b32_e32 v214, 0xffff0000, v214
	v_fma_f32 v40, v40, v100, v128
	v_fma_f32 v41, v41, v101, v214
	v_lshlrev_b32_e32 v128, 16, v215
	v_and_b32_e32 v215, 0xffff0000, v215
	v_fma_f32 v42, v42, v102, v128
	v_fma_f32 v43, v43, v103, v215
	v_mul_f32_e32 v214, v41, v41
	v_mul_f32_e32 v215, v43, v43
	v_fmac_f32_e32 v214, v40, v40
	v_fmac_f32_e32 v215, v42, v42
	v_add_f32_e32 v214, v214, v215
	v_add_f32_e32 v128, v212, v214
	v_cvt_pk_bf16_f32 v212, v44, v45
	v_cvt_pk_bf16_f32 v213, v46, v47
	v_cvt_pk_bf16_f32 v214, v40, v41
	v_cvt_pk_bf16_f32 v215, v42, v43
	v_mov_b32_e32 v44, v128
	global_store_dwordx4 v[174:175], v[212:215], off offset:-2048
	v_lshlrev_b32_e32 v128, 16, v216
	v_and_b32_e32 v216, 0xffff0000, v216
	v_fma_f32 v36, v36, v92, v128
	v_fma_f32 v37, v37, v93, v216
	v_lshlrev_b32_e32 v128, 16, v217
	v_and_b32_e32 v217, 0xffff0000, v217
	v_fma_f32 v38, v38, v94, v128
	v_fma_f32 v39, v39, v95, v217
	v_mul_f32_e32 v216, v37, v37
	v_mul_f32_e32 v217, v39, v39
	v_fmac_f32_e32 v216, v36, v36
	v_fmac_f32_e32 v217, v38, v38
	v_add_f32_e32 v216, v216, v217
	v_lshlrev_b32_e32 v128, 16, v218
	v_and_b32_e32 v218, 0xffff0000, v218
	v_fma_f32 v32, v32, v88, v128
	v_fma_f32 v33, v33, v89, v218
	v_lshlrev_b32_e32 v128, 16, v219
	v_and_b32_e32 v219, 0xffff0000, v219
	v_fma_f32 v34, v34, v90, v128
	v_fma_f32 v35, v35, v91, v219
	v_mul_f32_e32 v218, v33, v33
	v_mul_f32_e32 v219, v35, v35
	v_fmac_f32_e32 v218, v32, v32
	v_fmac_f32_e32 v219, v34, v34
	v_add_f32_e32 v218, v218, v219
	v_add_f32_e32 v128, v44, v216
	v_add_f32_e32 v128, v128, v218
	v_cvt_pk_bf16_f32 v216, v36, v37
	v_cvt_pk_bf16_f32 v217, v38, v39
	v_cvt_pk_bf16_f32 v218, v32, v33
	v_cvt_pk_bf16_f32 v219, v34, v35
	v_mov_b32_e32 v44, v128
	global_store_dwordx4 v[192:193], v[216:219], off offset:-2048
	v_lshlrev_b32_e32 v128, 16, v220
	v_and_b32_e32 v220, 0xffff0000, v220
	v_fma_f32 v28, v28, v108, v128
	v_fma_f32 v29, v29, v109, v220
	v_lshlrev_b32_e32 v128, 16, v221
	v_and_b32_e32 v221, 0xffff0000, v221
	v_fma_f32 v30, v30, v110, v128
	v_fma_f32 v31, v31, v111, v221
	v_mul_f32_e32 v220, v29, v29
	v_mul_f32_e32 v221, v31, v31
	v_fmac_f32_e32 v220, v28, v28
	v_fmac_f32_e32 v221, v30, v30
	v_add_f32_e32 v220, v220, v221
	v_lshlrev_b32_e32 v128, 16, v222
	v_and_b32_e32 v222, 0xffff0000, v222
	v_fma_f32 v24, v24, v100, v128
	v_fma_f32 v25, v25, v101, v222
	v_lshlrev_b32_e32 v128, 16, v223
	v_and_b32_e32 v223, 0xffff0000, v223
	v_fma_f32 v26, v26, v102, v128
	v_fma_f32 v27, v27, v103, v223
	v_mul_f32_e32 v222, v25, v25
	v_mul_f32_e32 v223, v27, v27
	v_fmac_f32_e32 v222, v24, v24
	v_fmac_f32_e32 v223, v26, v26
	v_add_f32_e32 v222, v222, v223
	v_add_f32_e32 v128, v220, v222
	v_cvt_pk_bf16_f32 v220, v28, v29
	v_cvt_pk_bf16_f32 v221, v30, v31
	v_cvt_pk_bf16_f32 v222, v24, v25
	v_cvt_pk_bf16_f32 v223, v26, v27
	v_mov_b32_e32 v28, v128
	global_store_dwordx4 v[174:175], v[220:223], off
	v_lshlrev_b32_e32 v128, 16, v224
	v_and_b32_e32 v224, 0xffff0000, v224
	v_fma_f32 v20, v20, v92, v128
	v_fma_f32 v21, v21, v93, v224
	v_lshlrev_b32_e32 v128, 16, v225
	v_and_b32_e32 v225, 0xffff0000, v225
	v_fma_f32 v22, v22, v94, v128
	v_fma_f32 v23, v23, v95, v225
	v_mul_f32_e32 v224, v21, v21
	v_mul_f32_e32 v225, v23, v23
	v_fmac_f32_e32 v224, v20, v20
	v_fmac_f32_e32 v225, v22, v22
	v_add_f32_e32 v224, v224, v225
	v_lshlrev_b32_e32 v128, 16, v226
	v_and_b32_e32 v226, 0xffff0000, v226
	v_fma_f32 v16, v16, v88, v128
	v_fma_f32 v17, v17, v89, v226
	v_lshlrev_b32_e32 v128, 16, v227
	v_and_b32_e32 v227, 0xffff0000, v227
	v_fma_f32 v18, v18, v90, v128
	v_fma_f32 v19, v19, v91, v227
	v_mul_f32_e32 v226, v17, v17
	v_mul_f32_e32 v227, v19, v19
	v_fmac_f32_e32 v226, v16, v16
	v_fmac_f32_e32 v227, v18, v18
	v_add_f32_e32 v226, v226, v227
	v_add_f32_e32 v128, v28, v224
	v_add_f32_e32 v128, v128, v226
	v_cvt_pk_bf16_f32 v224, v20, v21
	v_cvt_pk_bf16_f32 v225, v22, v23
	v_cvt_pk_bf16_f32 v226, v16, v17
	v_cvt_pk_bf16_f32 v227, v18, v19
	v_mov_b32_e32 v28, v128
	global_store_dwordx4 v[192:193], v[224:227], off
	s_waitcnt vmcnt(12)
; __device__ __forceinline__ unsigned cvt_pk_bf16(float lo, float hi) { const f32x2_t v = {lo, hi}; const bf16x2_t b = __builtin_convertvector(v, bf16x2_t); return __builtin_bit_cast(unsigned, b); }
;     __device__ __forceinline__ void operator()(const f32x4 (&acc)[2][2][4][2], const Unit& u, int wr, int wc, int fr, int fq, int ui) const {
;     ...
;                     const unsigned p0 = xb[g % 3][bj][2 * n], p1 = xb[g % 3][bj][2 * n + 1];
;                     const f32x4 xo = {__builtin_bit_cast(float, p0 << 16), __builtin_bit_cast(float, p0 & 0xFFFF0000u), __builtin_bit_cast(float, p1 << 16), __builtin_bit_cast(float, p1 & 0xFFFF0000u)};
;                     const f32x4 xn = xo + cr[bj][n] * acc[ai][bj][m][n];
;                     sq += (xn[0] * xn[0] + xn[1] * xn[1]) + (xn[2] * xn[2] + xn[3] * xn[3]);
;                     if (n == 0) { xs.x = cvt_pk_bf16(xn[0], xn[1]); xs.y = cvt_pk_bf16(xn[2], xn[3]); } else { xs.z = cvt_pk_bf16(xn[0], xn[1]); xs.w = cvt_pk_bf16(xn[2], xn[3]); }
;                 }
;                 *(u32x4*)(x + EPIRES_OFF(g, bj)) = xs;
;             }
;             sq += __shfl_xor(sq, 16); sq += __shfl_xor(sq, 32);
;             if (fq == 0) ss[(size_t)row_ * 32 + u.pn * 4 + wc] = sq;
	v_lshlrev_b32_e32 v128, 16, v138
	v_and_b32_e32 v138, 0xffff0000, v138
	v_fma_f32 v12, v12, v108, v128
	v_fma_f32 v13, v13, v109, v138
	v_lshlrev_b32_e32 v128, 16, v139
	v_and_b32_e32 v139, 0xffff0000, v139
	v_fma_f32 v14, v14, v110, v128
	v_fma_f32 v15, v15, v111, v139
	v_mul_f32_e32 v138, v13, v13
	v_mul_f32_e32 v139, v15, v15
	v_fmac_f32_e32 v138, v12, v12
	v_fmac_f32_e32 v139, v14, v14
	v_add_f32_e32 v138, v138, v139
	v_lshlrev_b32_e32 v128, 16, v140
	v_and_b32_e32 v140, 0xffff0000, v140
	v_fma_f32 v8, v8, v100, v128
	v_fma_f32 v9, v9, v101, v140
	v_lshlrev_b32_e32 v128, 16, v141
	v_and_b32_e32 v141, 0xffff0000, v141
	v_fma_f32 v10, v10, v102, v128
	v_fma_f32 v11, v11, v103, v141
	v_mul_f32_e32 v140, v9, v9
	v_mul_f32_e32 v141, v11, v11
	v_fmac_f32_e32 v140, v8, v8
	v_fmac_f32_e32 v141, v10, v10
	v_add_f32_e32 v140, v140, v141
	v_add_f32_e32 v128, v138, v140
	v_cvt_pk_bf16_f32 v138, v12, v13
	v_cvt_pk_bf16_f32 v139, v14, v15
	v_cvt_pk_bf16_f32 v140, v8, v9
	v_cvt_pk_bf16_f32 v141, v10, v11
	v_mov_b32_e32 v12, v128
	global_store_dwordx4 v[174:175], v[138:141], off offset:2048
	v_lshlrev_b32_e32 v128, 16, v134
	v_and_b32_e32 v134, 0xffff0000, v134
	v_fma_f32 v4, v4, v92, v128
	v_fma_f32 v5, v5, v93, v134
	v_lshlrev_b32_e32 v128, 16, v135
	v_and_b32_e32 v135, 0xffff0000, v135
	v_fma_f32 v6, v6, v94, v128
	v_fma_f32 v7, v7, v95, v135
	v_mul_f32_e32 v134, v5, v5
	v_mul_f32_e32 v135, v7, v7
	v_fmac_f32_e32 v134, v4, v4
	v_fmac_f32_e32 v135, v6, v6
	v_add_f32_e32 v134, v134, v135
	v_lshlrev_b32_e32 v128, 16, v136
	v_and_b32_e32 v136, 0xffff0000, v136
	v_fma_f32 v0, v0, v88, v128
	v_fma_f32 v1, v1, v89, v136
	v_lshlrev_b32_e32 v128, 16, v137
	v_and_b32_e32 v137, 0xffff0000, v137
	v_fma_f32 v2, v2, v90, v128
	v_fma_f32 v3, v3, v91, v137
	v_mul_f32_e32 v136, v1, v1
	v_mul_f32_e32 v137, v3, v3
	v_fmac_f32_e32 v136, v0, v0
	v_fmac_f32_e32 v137, v2, v2
	v_add_f32_e32 v136, v136, v137
	v_add_f32_e32 v128, v12, v134
	v_add_f32_e32 v128, v128, v136
	v_cvt_pk_bf16_f32 v134, v4, v5
	v_cvt_pk_bf16_f32 v135, v6, v7
	v_cvt_pk_bf16_f32 v136, v0, v1
	v_cvt_pk_bf16_f32 v137, v2, v3
	v_mov_b32_e32 v12, v128
	global_store_dwordx4 v[192:193], v[134:137], off offset:2048
	v_xor_b32_e32 v128, 16, v228
	v_add_u32_e32 v172, 64, v171
	v_xor_b32_e32 v173, 32, v228
	v_cmp_lt_i32_e32 vcc, v128, v172
	s_nop 1
	v_cndmask_b32_e32 v128, v228, v128, vcc
	v_cmp_lt_i32_e32 vcc, v173, v172
	v_lshlrev_b32_e32 v128, 2, v128
	v_lshl_add_u32 v190, s49, 8, v184
	v_cndmask_b32_e32 v172, v228, v173, vcc
	v_lshlrev_b32_e32 v196, 2, v172
	s_lshl_b32 s18, s48, 2
	s_ashr_i32 s19, s18, 31
	ds_bpermute_b32 v146, v128, v142
	ds_bpermute_b32 v147, v128, v124
	ds_bpermute_b32 v148, v128, v104
	ds_bpermute_b32 v149, v128, v76
	ds_bpermute_b32 v150, v128, v60
	ds_bpermute_b32 v151, v128, v44
	ds_bpermute_b32 v152, v128, v28
	ds_bpermute_b32 v153, v128, v12
	s_waitcnt lgkmcnt(0)
	v_add_f32_e32 v142, v142, v146
	v_add_f32_e32 v124, v124, v147
	v_add_f32_e32 v104, v104, v148
	v_add_f32_e32 v76, v76, v149
	v_add_f32_e32 v60, v60, v150
	v_add_f32_e32 v44, v44, v151
	v_add_f32_e32 v28, v28, v152
	v_add_f32_e32 v12, v12, v153
	ds_bpermute_b32 v146, v196, v142
	ds_bpermute_b32 v147, v196, v124
	ds_bpermute_b32 v148, v196, v104
	ds_bpermute_b32 v149, v196, v76
	ds_bpermute_b32 v150, v196, v60
	ds_bpermute_b32 v151, v196, v44
	ds_bpermute_b32 v152, v196, v28
	ds_bpermute_b32 v153, v196, v12
	s_and_saveexec_b64 s[20:21], s[4:5]
	s_waitcnt lgkmcnt(0)
	s_lshl_b32 s64, s36, 2
	v_add_f32_e32 v142, v142, v146
	v_or_b32_e32 v154, 0, v190
	v_ashrrev_i32_e32 v155, 31, v154
	v_lshlrev_b64 v[154:155], 7, v[154:155]
	v_lshl_add_u64 v[154:155], s[12:13], 0, v[154:155]
	v_lshl_add_u64 v[154:155], s[18:19], 2, v[154:155]
	v_lshl_add_u64 v[154:155], v[154:155], 0, s[64:65]
	global_store_dword v[154:155], v142, off
	v_add_f32_e32 v124, v124, v147
	v_or_b32_e32 v154, 16, v190
	v_ashrrev_i32_e32 v155, 31, v154
	v_lshlrev_b64 v[154:155], 7, v[154:155]
	v_lshl_add_u64 v[154:155], s[12:13], 0, v[154:155]
	v_lshl_add_u64 v[154:155], s[18:19], 2, v[154:155]
	v_lshl_add_u64 v[154:155], v[154:155], 0, s[64:65]
	global_store_dword v[154:155], v124, off
	v_add_f32_e32 v104, v104, v148
	v_or_b32_e32 v154, 32, v190
	v_ashrrev_i32_e32 v155, 31, v154
	v_lshlrev_b64 v[154:155], 7, v[154:155]
	v_lshl_add_u64 v[154:155], s[12:13], 0, v[154:155]
	v_lshl_add_u64 v[154:155], s[18:19], 2, v[154:155]
	v_lshl_add_u64 v[154:155], v[154:155], 0, s[64:65]
	global_store_dword v[154:155], v104, off
	v_add_f32_e32 v76, v76, v149
	v_or_b32_e32 v154, 48, v190
	v_ashrrev_i32_e32 v155, 31, v154
	v_lshlrev_b64 v[154:155], 7, v[154:155]
	v_lshl_add_u64 v[154:155], s[12:13], 0, v[154:155]
	v_lshl_add_u64 v[154:155], s[18:19], 2, v[154:155]
	v_lshl_add_u64 v[154:155], v[154:155], 0, s[64:65]
	global_store_dword v[154:155], v76, off
	v_add_f32_e32 v60, v60, v150
	v_or_b32_e32 v154, 128, v190
	v_ashrrev_i32_e32 v155, 31, v154
	v_lshlrev_b64 v[154:155], 7, v[154:155]
	v_lshl_add_u64 v[154:155], s[12:13], 0, v[154:155]
	v_lshl_add_u64 v[154:155], s[18:19], 2, v[154:155]
	v_lshl_add_u64 v[154:155], v[154:155], 0, s[64:65]
	global_store_dword v[154:155], v60, off
	v_add_f32_e32 v44, v44, v151
	v_or_b32_e32 v154, 144, v190
	v_ashrrev_i32_e32 v155, 31, v154
	v_lshlrev_b64 v[154:155], 7, v[154:155]
	v_lshl_add_u64 v[154:155], s[12:13], 0, v[154:155]
	v_lshl_add_u64 v[154:155], s[18:19], 2, v[154:155]
	v_lshl_add_u64 v[154:155], v[154:155], 0, s[64:65]
	global_store_dword v[154:155], v44, off
	v_add_f32_e32 v28, v28, v152
	v_or_b32_e32 v154, 160, v190
	v_ashrrev_i32_e32 v155, 31, v154
	v_lshlrev_b64 v[154:155], 7, v[154:155]
	v_lshl_add_u64 v[154:155], s[12:13], 0, v[154:155]
	v_lshl_add_u64 v[154:155], s[18:19], 2, v[154:155]
	v_lshl_add_u64 v[154:155], v[154:155], 0, s[64:65]
	global_store_dword v[154:155], v28, off
	v_add_f32_e32 v12, v12, v153
	v_or_b32_e32 v154, 176, v190
	v_ashrrev_i32_e32 v155, 31, v154
	v_lshlrev_b64 v[154:155], 7, v[154:155]
	v_lshl_add_u64 v[154:155], s[12:13], 0, v[154:155]
	v_lshl_add_u64 v[154:155], s[18:19], 2, v[154:155]
	v_lshl_add_u64 v[154:155], v[154:155], 0, s[64:65]
	global_store_dword v[154:155], v12, off
